# baseline (speedup 1.0000x reference)
_Z6k_prepPK15HIP_vector_typeIfLj4EEPS_IjLj4EEiPKfS6_S6_S6_PtS7_PS_IfLj2EE:
	s_cmp_lt_u32 s2, 0x400
	s_cbranch_scc1 .Lprep_w
	s_sub_u32 s2, s2, 0x400
	s_branch .Lprep_go
.Lprep_w:
	s_add_u32 s2, s2, 0x800
.Lprep_go:
	s_mov_b64 s[4:5], -1
	s_cmpk_lt_u32 s2, 0x800
	v_and_b32_e32 v1, 63, v0
	s_cbranch_scc0 .LBB0_2
	s_load_dwordx4 s[4:7], s[0:1], 0x0
	v_lshlrev_b32_e32 v2, 3, v0
	v_and_b32_e32 v2, 0x600, v2
	v_mov_b32_e32 v35, 0
	v_lshl_or_b32 v34, s2, 11, v2
	s_waitcnt lgkmcnt(0)
	v_lshl_add_u64 v[2:3], v[34:35], 4, s[4:5]
	v_lshlrev_b32_e32 v4, 4, v1
	v_mov_b32_e32 v5, v35
	v_lshl_add_u64 v[18:19], v[2:3], 0, v[4:5]
	s_movk_i32 s3, 0x1000
	v_add_co_u32_e32 v36, vcc, s3, v18
	global_load_dwordx4 v[2:5], v[18:19], off nt
	global_load_dwordx4 v[6:9], v[18:19], off offset:1024 nt
	global_load_dwordx4 v[10:13], v[18:19], off offset:2048 nt
	global_load_dwordx4 v[14:17], v[18:19], off offset:3072 nt
	v_addc_co_u32_e32 v37, vcc, 0, v19, vcc
	global_load_dwordx4 v[18:21], v[36:37], off nt
	global_load_dwordx4 v[22:25], v[36:37], off offset:1024 nt
	global_load_dwordx4 v[26:29], v[36:37], off offset:2048 nt
	global_load_dwordx4 v[30:33], v[36:37], off offset:3072 nt
	v_mov_b32_e32 v38, v35
	v_mov_b32_e32 v39, v35
	v_mov_b32_e32 v40, v35
	v_mov_b32_e32 v41, v35
	v_mov_b32_e32 v42, v35
	v_mov_b32_e32 v43, v35
	v_mov_b32_e32 v44, v35
	v_lshl_add_u64 v[36:37], v[34:35], 2, s[6:7]
	v_lshlrev_b32_e32 v34, 2, v1
	v_lshl_add_u64 v[36:37], v[36:37], 0, v[34:35]
	s_mov_b64 s[4:5], 0
	s_waitcnt vmcnt(7)
	v_cvt_pk_fp8_f32 v38, v2, v3
	s_waitcnt vmcnt(6)
	v_cvt_pk_fp8_f32 v39, v6, v7
	s_waitcnt vmcnt(5)
	v_cvt_pk_fp8_f32 v40, v10, v11
	s_waitcnt vmcnt(4)
	v_cvt_pk_fp8_f32 v41, v14, v15
	s_waitcnt vmcnt(3)
	v_cvt_pk_fp8_f32 v42, v18, v19
	s_waitcnt vmcnt(2)
	v_cvt_pk_fp8_f32 v43, v22, v23
	s_waitcnt vmcnt(1)
	v_cvt_pk_fp8_f32 v44, v26, v27
	s_waitcnt vmcnt(0)
	v_cvt_pk_fp8_f32 v35, v30, v31
	v_cvt_pk_fp8_f32 v38, v4, v5 op_sel:[0,0,1]
	v_cvt_pk_fp8_f32 v39, v8, v9 op_sel:[0,0,1]
	v_cvt_pk_fp8_f32 v40, v12, v13 op_sel:[0,0,1]
	v_cvt_pk_fp8_f32 v41, v16, v17 op_sel:[0,0,1]
	v_cvt_pk_fp8_f32 v42, v20, v21 op_sel:[0,0,1]
	v_cvt_pk_fp8_f32 v43, v24, v25 op_sel:[0,0,1]
	v_cvt_pk_fp8_f32 v44, v28, v29 op_sel:[0,0,1]
	v_cvt_pk_fp8_f32 v35, v32, v33 op_sel:[0,0,1]
	global_store_dword v[36:37], v38, off
	global_store_dword v[36:37], v39, off offset:256
	global_store_dword v[36:37], v40, off offset:512
	global_store_dword v[36:37], v41, off offset:768
	global_store_dword v[36:37], v42, off offset:1024
	global_store_dword v[36:37], v43, off offset:1280
	global_store_dword v[36:37], v44, off offset:1536
	global_store_dword v[36:37], v35, off offset:1792
